# v11 + GEMM accumulator zero-init with 64 v_mov_b64 (inline 0) instead of 127 v_mov_b32 copies
# speedup vs baseline: 1.0102x; 1.0078x over previous
.LBB0_248:
	s_xor_b64 s[10:11], s[30:31], -1
	s_and_b64 s[20:21], s[30:31], exec
	s_cselect_b32 s3, s7, s27
	s_cselect_b32 s5, s6, s26
	s_cselect_b32 s20, s9, s47
	s_cselect_b32 s21, s8, s46
	s_add_u32 s26, s26, 0x40080
	s_addc_u32 s27, s27, 0
	s_add_u32 s22, s46, 0x100
	v_mov_b32_e32 v2, 0
	s_addc_u32 s25, s47, 0
	s_mov_b32 s30, -2
	v_mov_b64_e32 v[2:3], 0
	v_mov_b64_e32 v[4:5], 0
	v_mov_b64_e32 v[6:7], 0
	v_mov_b64_e32 v[8:9], 0
	v_mov_b64_e32 v[10:11], 0
	v_mov_b64_e32 v[12:13], 0
	v_mov_b64_e32 v[14:15], 0
	v_mov_b64_e32 v[16:17], 0
	v_mov_b64_e32 v[18:19], 0
	v_mov_b64_e32 v[20:21], 0
	v_mov_b64_e32 v[22:23], 0
	v_mov_b64_e32 v[24:25], 0
	v_mov_b64_e32 v[26:27], 0
	v_mov_b64_e32 v[28:29], 0
	v_mov_b64_e32 v[30:31], 0
	v_mov_b64_e32 v[32:33], 0
	v_mov_b64_e32 v[34:35], 0
	v_mov_b64_e32 v[36:37], 0
	v_mov_b64_e32 v[38:39], 0
	v_mov_b64_e32 v[40:41], 0
	v_mov_b64_e32 v[42:43], 0
	v_mov_b64_e32 v[44:45], 0
	v_mov_b64_e32 v[46:47], 0
	v_mov_b64_e32 v[48:49], 0
	v_mov_b64_e32 v[54:55], 0
	v_mov_b64_e32 v[56:57], 0
	v_mov_b64_e32 v[58:59], 0
	v_mov_b64_e32 v[60:61], 0
	v_mov_b64_e32 v[62:63], 0
	v_mov_b64_e32 v[64:65], 0
	v_mov_b64_e32 v[66:67], 0
	v_mov_b64_e32 v[68:69], 0
	v_mov_b64_e32 v[70:71], 0
	v_mov_b64_e32 v[72:73], 0
	v_mov_b64_e32 v[74:75], 0
	v_mov_b64_e32 v[76:77], 0
	v_mov_b64_e32 v[78:79], 0
	v_mov_b64_e32 v[80:81], 0
	v_mov_b64_e32 v[82:83], 0
	v_mov_b64_e32 v[84:85], 0
	v_mov_b64_e32 v[86:87], 0
	v_mov_b64_e32 v[88:89], 0
	v_mov_b64_e32 v[90:91], 0
	v_mov_b64_e32 v[92:93], 0
	v_mov_b64_e32 v[94:95], 0
	v_mov_b64_e32 v[96:97], 0
	v_mov_b64_e32 v[98:99], 0
	v_mov_b64_e32 v[100:101], 0
	v_mov_b64_e32 v[102:103], 0
	v_mov_b64_e32 v[104:105], 0
	v_mov_b64_e32 v[106:107], 0
	v_mov_b64_e32 v[108:109], 0
	v_mov_b64_e32 v[110:111], 0
	v_mov_b64_e32 v[112:113], 0
	v_mov_b64_e32 v[114:115], 0
	v_mov_b64_e32 v[116:117], 0
	v_mov_b64_e32 v[118:119], 0
	v_mov_b64_e32 v[120:121], 0
	v_mov_b64_e32 v[122:123], 0
	v_mov_b64_e32 v[124:125], 0
	v_mov_b64_e32 v[126:127], 0
	v_mov_b64_e32 v[128:129], 0
	v_mov_b64_e32 v[164:165], 0
	v_mov_b64_e32 v[166:167], 0

.LBB0_277:
	s_xor_b64 s[56:57], s[10:11], -1
	s_and_b64 s[10:11], s[10:11], exec
	s_cselect_b32 s3, s53, s5
	s_cselect_b32 s9, s52, s4
	s_cselect_b32 s12, s55, s7
	s_cselect_b32 s13, s54, s6
	s_add_u32 s4, s4, 0x40080
	s_addc_u32 s5, s5, 0
	s_add_u32 s15, s6, 0x100
	s_waitcnt lgkmcnt(0)
	v_mov_b32_e32 v4, 0
	s_addc_u32 s16, s7, 0
	s_mov_b32 s17, -2
	v_mov_b64_e32 v[4:5], 0
	v_mov_b64_e32 v[6:7], 0
	v_mov_b64_e32 v[8:9], 0
	v_mov_b64_e32 v[10:11], 0
	v_mov_b64_e32 v[12:13], 0
	v_mov_b64_e32 v[14:15], 0
	v_mov_b64_e32 v[16:17], 0
	v_mov_b64_e32 v[18:19], 0
	v_mov_b64_e32 v[20:21], 0
	v_mov_b64_e32 v[22:23], 0
	v_mov_b64_e32 v[24:25], 0
	v_mov_b64_e32 v[26:27], 0
	v_mov_b64_e32 v[28:29], 0
	v_mov_b64_e32 v[30:31], 0
	v_mov_b64_e32 v[32:33], 0
	v_mov_b64_e32 v[34:35], 0
	v_mov_b64_e32 v[36:37], 0
	v_mov_b64_e32 v[38:39], 0
	v_mov_b64_e32 v[40:41], 0
	v_mov_b64_e32 v[42:43], 0
	v_mov_b64_e32 v[44:45], 0
	v_mov_b64_e32 v[46:47], 0
	v_mov_b64_e32 v[48:49], 0
	v_mov_b64_e32 v[50:51], 0
	v_mov_b64_e32 v[60:61], 0
	v_mov_b64_e32 v[62:63], 0
	v_mov_b64_e32 v[64:65], 0
	v_mov_b64_e32 v[66:67], 0
	v_mov_b64_e32 v[76:77], 0
	v_mov_b64_e32 v[78:79], 0
	v_mov_b64_e32 v[80:81], 0
	v_mov_b64_e32 v[82:83], 0
	v_mov_b64_e32 v[100:101], 0
	v_mov_b64_e32 v[102:103], 0
	v_mov_b64_e32 v[104:105], 0
	v_mov_b64_e32 v[106:107], 0
	v_mov_b64_e32 v[108:109], 0
	v_mov_b64_e32 v[110:111], 0
	v_mov_b64_e32 v[112:113], 0
	v_mov_b64_e32 v[114:115], 0
	v_mov_b64_e32 v[116:117], 0
	v_mov_b64_e32 v[118:119], 0
	v_mov_b64_e32 v[120:121], 0
	v_mov_b64_e32 v[122:123], 0
	v_mov_b64_e32 v[124:125], 0
	v_mov_b64_e32 v[126:127], 0
	v_mov_b64_e32 v[128:129], 0
	v_mov_b64_e32 v[130:131], 0
	v_mov_b64_e32 v[132:133], 0
	v_mov_b64_e32 v[134:135], 0
	v_mov_b64_e32 v[136:137], 0
	v_mov_b64_e32 v[138:139], 0
	v_mov_b64_e32 v[144:145], 0
	v_mov_b64_e32 v[146:147], 0
	v_mov_b64_e32 v[148:149], 0
	v_mov_b64_e32 v[150:151], 0
	v_mov_b64_e32 v[152:153], 0
	v_mov_b64_e32 v[154:155], 0
	v_mov_b64_e32 v[156:157], 0
	v_mov_b64_e32 v[158:159], 0
	v_mov_b64_e32 v[160:161], 0
	v_mov_b64_e32 v[162:163], 0
	v_mov_b64_e32 v[164:165], 0
	v_mov_b64_e32 v[166:167], 0

.LBB0_1502:
	s_add_u32 s2, s2, 0x40080
	s_addc_u32 s3, s3, 0
	s_add_u32 s7, s34, 0x100
	v_mov_b32_e32 v0, 0
	s_addc_u32 s20, s35, 0
	s_mov_b32 s22, -2
	v_mov_b64_e32 v[0:1], 0
	v_mov_b64_e32 v[2:3], 0
	v_mov_b64_e32 v[4:5], 0
	v_mov_b64_e32 v[6:7], 0
	v_mov_b64_e32 v[8:9], 0
	v_mov_b64_e32 v[10:11], 0
	v_mov_b64_e32 v[12:13], 0
	v_mov_b64_e32 v[14:15], 0
	v_mov_b64_e32 v[16:17], 0
	v_mov_b64_e32 v[18:19], 0
	v_mov_b64_e32 v[20:21], 0
	v_mov_b64_e32 v[22:23], 0
	v_mov_b64_e32 v[24:25], 0
	v_mov_b64_e32 v[26:27], 0
	v_mov_b64_e32 v[28:29], 0
	v_mov_b64_e32 v[30:31], 0
	v_mov_b64_e32 v[32:33], 0
	v_mov_b64_e32 v[34:35], 0
	v_mov_b64_e32 v[36:37], 0
	v_mov_b64_e32 v[38:39], 0
	v_mov_b64_e32 v[40:41], 0
	v_mov_b64_e32 v[42:43], 0
	v_mov_b64_e32 v[44:45], 0
	v_mov_b64_e32 v[46:47], 0
	v_mov_b64_e32 v[48:49], 0
	v_mov_b64_e32 v[50:51], 0
	v_mov_b64_e32 v[52:53], 0
	v_mov_b64_e32 v[54:55], 0
	v_mov_b64_e32 v[56:57], 0
	v_mov_b64_e32 v[58:59], 0
	v_mov_b64_e32 v[60:61], 0
	v_mov_b64_e32 v[62:63], 0
	v_mov_b64_e32 v[64:65], 0
	v_mov_b64_e32 v[66:67], 0
	v_mov_b64_e32 v[68:69], 0
	v_mov_b64_e32 v[70:71], 0
	v_mov_b64_e32 v[72:73], 0
	v_mov_b64_e32 v[74:75], 0
	v_mov_b64_e32 v[76:77], 0
	v_mov_b64_e32 v[78:79], 0
	v_mov_b64_e32 v[80:81], 0
	v_mov_b64_e32 v[82:83], 0
	v_mov_b64_e32 v[84:85], 0
	v_mov_b64_e32 v[86:87], 0
	v_mov_b64_e32 v[88:89], 0
	v_mov_b64_e32 v[90:91], 0
	v_mov_b64_e32 v[92:93], 0
	v_mov_b64_e32 v[94:95], 0
	v_mov_b64_e32 v[96:97], 0
	v_mov_b64_e32 v[98:99], 0
	v_mov_b64_e32 v[100:101], 0
	v_mov_b64_e32 v[102:103], 0
	v_mov_b64_e32 v[104:105], 0
	v_mov_b64_e32 v[106:107], 0
	v_mov_b64_e32 v[108:109], 0
	v_mov_b64_e32 v[110:111], 0
	v_mov_b64_e32 v[112:113], 0
	v_mov_b64_e32 v[114:115], 0
	v_mov_b64_e32 v[116:117], 0
	v_mov_b64_e32 v[118:119], 0
	v_mov_b64_e32 v[120:121], 0
	v_mov_b64_e32 v[122:123], 0
	v_mov_b64_e32 v[124:125], 0
	v_mov_b64_e32 v[126:127], 0

.LBB0_1943:
	s_add_u32 s8, s36, 0x100
	v_mov_b32_e32 v48, 0
	s_addc_u32 s23, s37, 0
	s_mov_b32 s60, -2
	s_mov_b64 s[36:37], s[16:17]
	v_mov_b64_e32 v[48:49], 0
	v_mov_b64_e32 v[50:51], 0
	v_mov_b64_e32 v[52:53], 0
	v_mov_b64_e32 v[54:55], 0
	v_mov_b64_e32 v[56:57], 0
	v_mov_b64_e32 v[58:59], 0
	v_mov_b64_e32 v[60:61], 0
	v_mov_b64_e32 v[62:63], 0
	v_mov_b64_e32 v[64:65], 0
	v_mov_b64_e32 v[66:67], 0
	v_mov_b64_e32 v[68:69], 0
	v_mov_b64_e32 v[70:71], 0
	v_mov_b64_e32 v[72:73], 0
	v_mov_b64_e32 v[74:75], 0
	v_mov_b64_e32 v[76:77], 0
	v_mov_b64_e32 v[78:79], 0
	v_mov_b64_e32 v[80:81], 0
	v_mov_b64_e32 v[82:83], 0
	v_mov_b64_e32 v[84:85], 0
	v_mov_b64_e32 v[86:87], 0
	v_mov_b64_e32 v[88:89], 0
	v_mov_b64_e32 v[90:91], 0
	v_mov_b64_e32 v[92:93], 0
	v_mov_b64_e32 v[94:95], 0
	v_mov_b64_e32 v[96:97], 0
	v_mov_b64_e32 v[98:99], 0
	v_mov_b64_e32 v[100:101], 0
	v_mov_b64_e32 v[102:103], 0
	v_mov_b64_e32 v[104:105], 0
	v_mov_b64_e32 v[106:107], 0
	v_mov_b64_e32 v[108:109], 0
	v_mov_b64_e32 v[110:111], 0
	v_mov_b64_e32 v[112:113], 0
	v_mov_b64_e32 v[114:115], 0
	v_mov_b64_e32 v[116:117], 0
	v_mov_b64_e32 v[118:119], 0
	v_mov_b64_e32 v[120:121], 0
	v_mov_b64_e32 v[122:123], 0
	v_mov_b64_e32 v[124:125], 0
	v_mov_b64_e32 v[126:127], 0
	v_mov_b64_e32 v[128:129], 0
	v_mov_b64_e32 v[130:131], 0
	v_mov_b64_e32 v[132:133], 0
	v_mov_b64_e32 v[134:135], 0
	v_mov_b64_e32 v[136:137], 0
	v_mov_b64_e32 v[138:139], 0
	v_mov_b64_e32 v[140:141], 0
	v_mov_b64_e32 v[142:143], 0
	v_mov_b64_e32 v[144:145], 0
	v_mov_b64_e32 v[146:147], 0
	v_mov_b64_e32 v[148:149], 0
	v_mov_b64_e32 v[150:151], 0
	v_mov_b64_e32 v[152:153], 0
	v_mov_b64_e32 v[154:155], 0
	v_mov_b64_e32 v[156:157], 0
	v_mov_b64_e32 v[158:159], 0
	v_mov_b64_e32 v[160:161], 0
	v_mov_b64_e32 v[162:163], 0
	v_mov_b64_e32 v[164:165], 0
	v_mov_b64_e32 v[166:167], 0
	v_mov_b64_e32 v[168:169], 0
	v_mov_b64_e32 v[170:171], 0
	v_mov_b64_e32 v[172:173], 0
	v_mov_b64_e32 v[174:175], 0
	s_branch .LBB0_1945

.LBB0_2381:
	s_add_u32 s16, s16, 0x30080
	s_addc_u32 s17, s17, 0
	s_add_u32 s52, s18, 0x100
	v_mov_b32_e32 v0, 0
	s_addc_u32 s53, s19, 0
	s_mov_b32 s54, -2
	v_mov_b64_e32 v[0:1], 0
	v_mov_b64_e32 v[2:3], 0
	v_mov_b64_e32 v[4:5], 0
	v_mov_b64_e32 v[6:7], 0
	v_mov_b64_e32 v[8:9], 0
	v_mov_b64_e32 v[10:11], 0
	v_mov_b64_e32 v[12:13], 0
	v_mov_b64_e32 v[14:15], 0
	v_mov_b64_e32 v[16:17], 0
	v_mov_b64_e32 v[18:19], 0
	v_mov_b64_e32 v[20:21], 0
	v_mov_b64_e32 v[22:23], 0
	v_mov_b64_e32 v[24:25], 0
	v_mov_b64_e32 v[26:27], 0
	v_mov_b64_e32 v[28:29], 0
	v_mov_b64_e32 v[30:31], 0
	v_mov_b64_e32 v[32:33], 0
	v_mov_b64_e32 v[34:35], 0
	v_mov_b64_e32 v[36:37], 0
	v_mov_b64_e32 v[38:39], 0
	v_mov_b64_e32 v[40:41], 0
	v_mov_b64_e32 v[42:43], 0
	v_mov_b64_e32 v[44:45], 0
	v_mov_b64_e32 v[46:47], 0
	v_mov_b64_e32 v[48:49], 0
	v_mov_b64_e32 v[50:51], 0
	v_mov_b64_e32 v[52:53], 0
	v_mov_b64_e32 v[54:55], 0
	v_mov_b64_e32 v[56:57], 0
	v_mov_b64_e32 v[58:59], 0
	v_mov_b64_e32 v[60:61], 0
	v_mov_b64_e32 v[62:63], 0
	v_mov_b64_e32 v[64:65], 0
	v_mov_b64_e32 v[66:67], 0
	v_mov_b64_e32 v[68:69], 0
	v_mov_b64_e32 v[70:71], 0
	v_mov_b64_e32 v[72:73], 0
	v_mov_b64_e32 v[74:75], 0
	v_mov_b64_e32 v[76:77], 0
	v_mov_b64_e32 v[78:79], 0
	v_mov_b64_e32 v[80:81], 0
	v_mov_b64_e32 v[82:83], 0
	v_mov_b64_e32 v[84:85], 0
	v_mov_b64_e32 v[86:87], 0
	v_mov_b64_e32 v[88:89], 0
	v_mov_b64_e32 v[90:91], 0
	v_mov_b64_e32 v[92:93], 0
	v_mov_b64_e32 v[94:95], 0
	v_mov_b64_e32 v[96:97], 0
	v_mov_b64_e32 v[98:99], 0
	v_mov_b64_e32 v[100:101], 0
	v_mov_b64_e32 v[102:103], 0
	v_mov_b64_e32 v[104:105], 0
	v_mov_b64_e32 v[106:107], 0
	v_mov_b64_e32 v[108:109], 0
	v_mov_b64_e32 v[110:111], 0
	v_mov_b64_e32 v[112:113], 0
	v_mov_b64_e32 v[114:115], 0
	v_mov_b64_e32 v[116:117], 0
	v_mov_b64_e32 v[118:119], 0
	v_mov_b64_e32 v[120:121], 0
	v_mov_b64_e32 v[122:123], 0
	v_mov_b64_e32 v[124:125], 0
	v_mov_b64_e32 v[126:127], 0

.LBB0_3993:
	v_mbcnt_lo_u32_b32 v2, -1, 0
	v_mbcnt_hi_u32_b32 v2, -1, v2
	s_lshl_b32 s22, s10, 8
	v_add_u32_e32 v0, s58, v2
	v_ashrrev_i32_e32 v0, 1, v0
	v_add_u32_e32 v0, s22, v0
	v_ashrrev_i32_e32 v1, 31, v0
	v_readlane_b32 s8, v253, 54
	v_lshlrev_b64 v[0:1], 6, v[0:1]
	v_readlane_b32 s9, v253, 55
	v_lshlrev_b32_e32 v2, 4, v2
	v_and_b32_e32 v170, 16, v2
	v_lshl_add_u64 v[0:1], s[8:9], 0, v[0:1]
	s_lshl_b32 s8, s23, 3
	s_ashr_i32 s9, s8, 31
	v_lshl_add_u64 v[0:1], s[8:9], 2, v[0:1]
	v_lshl_add_u64 v[0:1], v[0:1], 0, v[170:171]
	s_add_i32 m0, s3, 0x22000
	v_readlane_b32 s8, v252, 31
	global_load_lds_dwordx4 v[0:1], off
	v_mov_b32_e32 v123, 0
	v_readlane_b32 s9, v252, 32
	s_andn2_b64 vcc, exec, s[8:9]
	s_waitcnt vmcnt(0)
	v_mov_b64_e32 v[0:1], 0
	v_mov_b64_e32 v[2:3], 0
	v_mov_b64_e32 v[4:5], 0
	v_mov_b64_e32 v[6:7], 0
	v_mov_b64_e32 v[8:9], 0
	v_mov_b64_e32 v[10:11], 0
	v_mov_b64_e32 v[12:13], 0
	v_mov_b64_e32 v[14:15], 0
	v_mov_b64_e32 v[16:17], 0
	v_mov_b64_e32 v[18:19], 0
	v_mov_b64_e32 v[20:21], 0
	v_mov_b64_e32 v[22:23], 0
	v_mov_b64_e32 v[24:25], 0
	v_mov_b64_e32 v[26:27], 0
	v_mov_b64_e32 v[28:29], 0
	v_mov_b64_e32 v[30:31], 0
	v_mov_b64_e32 v[32:33], 0
	v_mov_b64_e32 v[34:35], 0
	v_mov_b64_e32 v[36:37], 0
	v_mov_b64_e32 v[38:39], 0
	v_mov_b64_e32 v[40:41], 0
	v_mov_b64_e32 v[42:43], 0
	v_mov_b64_e32 v[44:45], 0
	v_mov_b64_e32 v[46:47], 0
	v_mov_b64_e32 v[48:49], 0
	v_mov_b64_e32 v[50:51], 0
	v_mov_b64_e32 v[52:53], 0
	v_mov_b64_e32 v[54:55], 0
	v_mov_b64_e32 v[56:57], 0
	v_mov_b64_e32 v[58:59], 0
	v_mov_b64_e32 v[60:61], 0
	v_mov_b64_e32 v[62:63], 0
	v_mov_b64_e32 v[64:65], 0
	v_mov_b64_e32 v[66:67], 0
	v_mov_b64_e32 v[68:69], 0
	v_mov_b64_e32 v[70:71], 0
	v_mov_b64_e32 v[72:73], 0
	v_mov_b64_e32 v[74:75], 0
	v_mov_b64_e32 v[76:77], 0
	v_mov_b64_e32 v[78:79], 0
	v_mov_b64_e32 v[80:81], 0
	v_mov_b64_e32 v[82:83], 0
	v_mov_b64_e32 v[84:85], 0
	v_mov_b64_e32 v[86:87], 0
	v_mov_b64_e32 v[88:89], 0
	v_mov_b64_e32 v[90:91], 0
	v_mov_b64_e32 v[92:93], 0
	v_mov_b64_e32 v[94:95], 0
	v_mov_b64_e32 v[96:97], 0
	v_mov_b64_e32 v[98:99], 0
	v_mov_b64_e32 v[100:101], 0
	v_mov_b64_e32 v[102:103], 0
	v_mov_b64_e32 v[104:105], 0
	v_mov_b64_e32 v[106:107], 0
	v_mov_b64_e32 v[108:109], 0
	v_mov_b64_e32 v[110:111], 0
	v_mov_b64_e32 v[112:113], 0
	v_mov_b64_e32 v[114:115], 0
	v_mov_b64_e32 v[116:117], 0
	v_mov_b64_e32 v[118:119], 0
	v_mov_b64_e32 v[120:121], 0
	v_mov_b64_e32 v[122:123], 0
	v_mov_b64_e32 v[124:125], 0
	v_mov_b64_e32 v[126:127], 0
	s_cbranch_vccnz .LBB0_3996
	s_add_u32 s4, s4, 0x20080
	s_addc_u32 s5, s5, 0
	s_add_u32 s25, s6, 0x100
	v_mov_b32_e32 v0, 0
	s_addc_u32 s27, s7, 0
	s_mov_b32 s6, 0
	v_mov_b64_e32 v[0:1], 0
	v_mov_b64_e32 v[2:3], 0
	v_mov_b64_e32 v[4:5], 0
	v_mov_b64_e32 v[6:7], 0
	v_mov_b64_e32 v[8:9], 0
	v_mov_b64_e32 v[10:11], 0
	v_mov_b64_e32 v[12:13], 0
	v_mov_b64_e32 v[14:15], 0
	v_mov_b64_e32 v[16:17], 0
	v_mov_b64_e32 v[18:19], 0
	v_mov_b64_e32 v[20:21], 0
	v_mov_b64_e32 v[22:23], 0
	v_mov_b64_e32 v[24:25], 0
	v_mov_b64_e32 v[26:27], 0
	v_mov_b64_e32 v[28:29], 0
	v_mov_b64_e32 v[30:31], 0
	v_mov_b64_e32 v[32:33], 0
	v_mov_b64_e32 v[34:35], 0
	v_mov_b64_e32 v[36:37], 0
	v_mov_b64_e32 v[38:39], 0
	v_mov_b64_e32 v[40:41], 0
	v_mov_b64_e32 v[42:43], 0
	v_mov_b64_e32 v[44:45], 0
	v_mov_b64_e32 v[46:47], 0
	v_mov_b64_e32 v[48:49], 0
	v_mov_b64_e32 v[50:51], 0
	v_mov_b64_e32 v[52:53], 0
	v_mov_b64_e32 v[54:55], 0
	v_mov_b64_e32 v[56:57], 0
	v_mov_b64_e32 v[58:59], 0
	v_mov_b64_e32 v[60:61], 0
	v_mov_b64_e32 v[62:63], 0
	v_mov_b64_e32 v[64:65], 0
	v_mov_b64_e32 v[66:67], 0
	v_mov_b64_e32 v[68:69], 0
	v_mov_b64_e32 v[70:71], 0
	v_mov_b64_e32 v[72:73], 0
	v_mov_b64_e32 v[74:75], 0
	v_mov_b64_e32 v[76:77], 0
	v_mov_b64_e32 v[78:79], 0
	v_mov_b64_e32 v[80:81], 0
	v_mov_b64_e32 v[82:83], 0
	v_mov_b64_e32 v[84:85], 0
	v_mov_b64_e32 v[86:87], 0
	v_mov_b64_e32 v[88:89], 0
	v_mov_b64_e32 v[90:91], 0
	v_mov_b64_e32 v[92:93], 0
	v_mov_b64_e32 v[94:95], 0
	v_mov_b64_e32 v[96:97], 0
	v_mov_b64_e32 v[98:99], 0
	v_mov_b64_e32 v[100:101], 0
	v_mov_b64_e32 v[102:103], 0
	v_mov_b64_e32 v[104:105], 0
	v_mov_b64_e32 v[106:107], 0
	v_mov_b64_e32 v[108:109], 0
	v_mov_b64_e32 v[110:111], 0
	v_mov_b64_e32 v[112:113], 0
	v_mov_b64_e32 v[114:115], 0
	v_mov_b64_e32 v[116:117], 0
	v_mov_b64_e32 v[118:119], 0
	v_mov_b64_e32 v[120:121], 0
	v_mov_b64_e32 v[122:123], 0
	v_mov_b64_e32 v[124:125], 0
	v_mov_b64_e32 v[126:127], 0

.LBB0_4064:
	v_mbcnt_lo_u32_b32 v2, -1, 0
	v_mbcnt_hi_u32_b32 v2, -1, v2
	s_lshl_b32 s22, s10, 8
	v_add_u32_e32 v0, s58, v2
	v_ashrrev_i32_e32 v0, 1, v0
	v_add_u32_e32 v0, s22, v0
	v_ashrrev_i32_e32 v1, 31, v0
	v_readlane_b32 s8, v253, 54
	v_lshlrev_b64 v[0:1], 6, v[0:1]
	v_readlane_b32 s9, v253, 55
	v_lshlrev_b32_e32 v2, 4, v2
	v_and_b32_e32 v170, 16, v2
	v_lshl_add_u64 v[0:1], s[8:9], 0, v[0:1]
	s_lshl_b32 s8, s23, 3
	s_ashr_i32 s9, s8, 31
	v_lshl_add_u64 v[0:1], s[8:9], 2, v[0:1]
	v_lshl_add_u64 v[0:1], v[0:1], 0, v[170:171]
	s_add_i32 m0, s3, 0x22000
	v_readlane_b32 s8, v252, 31
	global_load_lds_dwordx4 v[0:1], off
	v_mov_b32_e32 v123, 0
	v_readlane_b32 s9, v252, 32
	s_andn2_b64 vcc, exec, s[8:9]
	s_waitcnt vmcnt(0)
	s_waitcnt vmcnt(0)
	v_mov_b64_e32 v[0:1], 0
	v_mov_b64_e32 v[2:3], 0
	v_mov_b64_e32 v[4:5], 0
	v_mov_b64_e32 v[6:7], 0
	v_mov_b64_e32 v[8:9], 0
	v_mov_b64_e32 v[10:11], 0
	v_mov_b64_e32 v[12:13], 0
	v_mov_b64_e32 v[14:15], 0
	v_mov_b64_e32 v[16:17], 0
	v_mov_b64_e32 v[18:19], 0
	v_mov_b64_e32 v[20:21], 0
	v_mov_b64_e32 v[22:23], 0
	v_mov_b64_e32 v[24:25], 0
	v_mov_b64_e32 v[26:27], 0
	v_mov_b64_e32 v[28:29], 0
	v_mov_b64_e32 v[30:31], 0
	v_mov_b64_e32 v[32:33], 0
	v_mov_b64_e32 v[34:35], 0
	v_mov_b64_e32 v[36:37], 0
	v_mov_b64_e32 v[38:39], 0
	v_mov_b64_e32 v[40:41], 0
	v_mov_b64_e32 v[42:43], 0
	v_mov_b64_e32 v[44:45], 0
	v_mov_b64_e32 v[46:47], 0
	v_mov_b64_e32 v[48:49], 0
	v_mov_b64_e32 v[50:51], 0
	v_mov_b64_e32 v[52:53], 0
	v_mov_b64_e32 v[54:55], 0
	v_mov_b64_e32 v[56:57], 0
	v_mov_b64_e32 v[58:59], 0
	v_mov_b64_e32 v[60:61], 0
	v_mov_b64_e32 v[62:63], 0
	v_mov_b64_e32 v[64:65], 0
	v_mov_b64_e32 v[66:67], 0
	v_mov_b64_e32 v[68:69], 0
	v_mov_b64_e32 v[70:71], 0
	v_mov_b64_e32 v[72:73], 0
	v_mov_b64_e32 v[74:75], 0
	v_mov_b64_e32 v[76:77], 0
	v_mov_b64_e32 v[78:79], 0
	v_mov_b64_e32 v[80:81], 0
	v_mov_b64_e32 v[82:83], 0
	v_mov_b64_e32 v[84:85], 0
	v_mov_b64_e32 v[86:87], 0
	v_mov_b64_e32 v[88:89], 0
	v_mov_b64_e32 v[90:91], 0
	v_mov_b64_e32 v[92:93], 0
	v_mov_b64_e32 v[94:95], 0
	v_mov_b64_e32 v[96:97], 0
	v_mov_b64_e32 v[98:99], 0
	v_mov_b64_e32 v[100:101], 0
	v_mov_b64_e32 v[102:103], 0
	v_mov_b64_e32 v[104:105], 0
	v_mov_b64_e32 v[106:107], 0
	v_mov_b64_e32 v[108:109], 0
	v_mov_b64_e32 v[110:111], 0
	v_mov_b64_e32 v[112:113], 0
	v_mov_b64_e32 v[114:115], 0
	v_mov_b64_e32 v[116:117], 0
	v_mov_b64_e32 v[118:119], 0
	v_mov_b64_e32 v[120:121], 0
	v_mov_b64_e32 v[122:123], 0
	v_mov_b64_e32 v[124:125], 0
	v_mov_b64_e32 v[126:127], 0
	s_cbranch_vccnz .LBB0_4067
	s_add_u32 s4, s4, 0x20080
	s_addc_u32 s5, s5, 0
	s_add_u32 s25, s6, 0x100
	v_mov_b32_e32 v0, 0
	s_addc_u32 s27, s7, 0
	s_mov_b32 s6, 0
	v_mov_b64_e32 v[0:1], 0
	v_mov_b64_e32 v[2:3], 0
	v_mov_b64_e32 v[4:5], 0
	v_mov_b64_e32 v[6:7], 0
	v_mov_b64_e32 v[8:9], 0
	v_mov_b64_e32 v[10:11], 0
	v_mov_b64_e32 v[12:13], 0
	v_mov_b64_e32 v[14:15], 0
	v_mov_b64_e32 v[16:17], 0
	v_mov_b64_e32 v[18:19], 0
	v_mov_b64_e32 v[20:21], 0
	v_mov_b64_e32 v[22:23], 0
	v_mov_b64_e32 v[24:25], 0
	v_mov_b64_e32 v[26:27], 0
	v_mov_b64_e32 v[28:29], 0
	v_mov_b64_e32 v[30:31], 0
	v_mov_b64_e32 v[32:33], 0
	v_mov_b64_e32 v[34:35], 0
	v_mov_b64_e32 v[36:37], 0
	v_mov_b64_e32 v[38:39], 0
	v_mov_b64_e32 v[40:41], 0
	v_mov_b64_e32 v[42:43], 0
	v_mov_b64_e32 v[44:45], 0
	v_mov_b64_e32 v[46:47], 0
	v_mov_b64_e32 v[48:49], 0
	v_mov_b64_e32 v[50:51], 0
	v_mov_b64_e32 v[52:53], 0
	v_mov_b64_e32 v[54:55], 0
	v_mov_b64_e32 v[56:57], 0
	v_mov_b64_e32 v[58:59], 0
	v_mov_b64_e32 v[60:61], 0
	v_mov_b64_e32 v[62:63], 0
	v_mov_b64_e32 v[64:65], 0
	v_mov_b64_e32 v[66:67], 0
	v_mov_b64_e32 v[68:69], 0
	v_mov_b64_e32 v[70:71], 0
	v_mov_b64_e32 v[72:73], 0
	v_mov_b64_e32 v[74:75], 0
	v_mov_b64_e32 v[76:77], 0
	v_mov_b64_e32 v[78:79], 0
	v_mov_b64_e32 v[80:81], 0
	v_mov_b64_e32 v[82:83], 0
	v_mov_b64_e32 v[84:85], 0
	v_mov_b64_e32 v[86:87], 0
	v_mov_b64_e32 v[88:89], 0
	v_mov_b64_e32 v[90:91], 0
	v_mov_b64_e32 v[92:93], 0
	v_mov_b64_e32 v[94:95], 0
	v_mov_b64_e32 v[96:97], 0
	v_mov_b64_e32 v[98:99], 0
	v_mov_b64_e32 v[100:101], 0
	v_mov_b64_e32 v[102:103], 0
	v_mov_b64_e32 v[104:105], 0
	v_mov_b64_e32 v[106:107], 0
	v_mov_b64_e32 v[108:109], 0
	v_mov_b64_e32 v[110:111], 0
	v_mov_b64_e32 v[112:113], 0
	v_mov_b64_e32 v[114:115], 0
	v_mov_b64_e32 v[116:117], 0
	v_mov_b64_e32 v[118:119], 0
	v_mov_b64_e32 v[120:121], 0
	v_mov_b64_e32 v[122:123], 0
	v_mov_b64_e32 v[124:125], 0
	v_mov_b64_e32 v[126:127], 0

.LBB0_4931:
	s_add_u32 s20, s20, 0x40080
	s_addc_u32 s21, s21, 0
	s_add_u32 s11, s22, 0x100
	v_mov_b32_e32 v0, 0
	s_addc_u32 s13, s23, 0
	s_mov_b32 s50, -2
	v_mov_b64_e32 v[0:1], 0
	v_mov_b64_e32 v[2:3], 0
	v_mov_b64_e32 v[4:5], 0
	v_mov_b64_e32 v[6:7], 0
	v_mov_b64_e32 v[8:9], 0
	v_mov_b64_e32 v[10:11], 0
	v_mov_b64_e32 v[12:13], 0
	v_mov_b64_e32 v[14:15], 0
	v_mov_b64_e32 v[16:17], 0
	v_mov_b64_e32 v[18:19], 0
	v_mov_b64_e32 v[20:21], 0
	v_mov_b64_e32 v[22:23], 0
	v_mov_b64_e32 v[24:25], 0
	v_mov_b64_e32 v[26:27], 0
	v_mov_b64_e32 v[28:29], 0
	v_mov_b64_e32 v[30:31], 0
	v_mov_b64_e32 v[32:33], 0
	v_mov_b64_e32 v[34:35], 0
	v_mov_b64_e32 v[36:37], 0
	v_mov_b64_e32 v[38:39], 0
	v_mov_b64_e32 v[40:41], 0
	v_mov_b64_e32 v[42:43], 0
	v_mov_b64_e32 v[44:45], 0
	v_mov_b64_e32 v[46:47], 0
	v_mov_b64_e32 v[48:49], 0
	v_mov_b64_e32 v[50:51], 0
	v_mov_b64_e32 v[52:53], 0
	v_mov_b64_e32 v[54:55], 0
	v_mov_b64_e32 v[56:57], 0
	v_mov_b64_e32 v[58:59], 0
	v_mov_b64_e32 v[60:61], 0
	v_mov_b64_e32 v[62:63], 0
	v_mov_b64_e32 v[64:65], 0
	v_mov_b64_e32 v[66:67], 0
	v_mov_b64_e32 v[68:69], 0
	v_mov_b64_e32 v[70:71], 0
	v_mov_b64_e32 v[72:73], 0
	v_mov_b64_e32 v[74:75], 0
	v_mov_b64_e32 v[76:77], 0
	v_mov_b64_e32 v[78:79], 0
	v_mov_b64_e32 v[80:81], 0
	v_mov_b64_e32 v[82:83], 0
	v_mov_b64_e32 v[84:85], 0
	v_mov_b64_e32 v[86:87], 0
	v_mov_b64_e32 v[88:89], 0
	v_mov_b64_e32 v[90:91], 0
	v_mov_b64_e32 v[92:93], 0
	v_mov_b64_e32 v[94:95], 0
	v_mov_b64_e32 v[96:97], 0
	v_mov_b64_e32 v[98:99], 0
	v_mov_b64_e32 v[100:101], 0
	v_mov_b64_e32 v[102:103], 0
	v_mov_b64_e32 v[104:105], 0
	v_mov_b64_e32 v[106:107], 0
	v_mov_b64_e32 v[108:109], 0
	v_mov_b64_e32 v[110:111], 0
	v_mov_b64_e32 v[112:113], 0
	v_mov_b64_e32 v[114:115], 0
	v_mov_b64_e32 v[116:117], 0
	v_mov_b64_e32 v[118:119], 0
	v_mov_b64_e32 v[120:121], 0
	v_mov_b64_e32 v[122:123], 0
	v_mov_b64_e32 v[124:125], 0
	v_mov_b64_e32 v[126:127], 0

.LBB0_5812:
	s_add_u32 s14, s14, 0x30080
	s_addc_u32 s15, s15, 0
	s_add_u32 s51, s16, 0x100
	v_mov_b32_e32 v0, 0
	s_addc_u32 s52, s17, 0
	s_mov_b32 s53, -2
	v_mov_b64_e32 v[0:1], 0
	v_mov_b64_e32 v[2:3], 0
	v_mov_b64_e32 v[4:5], 0
	v_mov_b64_e32 v[6:7], 0
	v_mov_b64_e32 v[8:9], 0
	v_mov_b64_e32 v[10:11], 0
	v_mov_b64_e32 v[12:13], 0
	v_mov_b64_e32 v[14:15], 0
	v_mov_b64_e32 v[16:17], 0
	v_mov_b64_e32 v[18:19], 0
	v_mov_b64_e32 v[20:21], 0
	v_mov_b64_e32 v[22:23], 0
	v_mov_b64_e32 v[24:25], 0
	v_mov_b64_e32 v[26:27], 0
	v_mov_b64_e32 v[28:29], 0
	v_mov_b64_e32 v[30:31], 0
	v_mov_b64_e32 v[32:33], 0
	v_mov_b64_e32 v[34:35], 0
	v_mov_b64_e32 v[36:37], 0
	v_mov_b64_e32 v[38:39], 0
	v_mov_b64_e32 v[40:41], 0
	v_mov_b64_e32 v[42:43], 0
	v_mov_b64_e32 v[44:45], 0
	v_mov_b64_e32 v[46:47], 0
	v_mov_b64_e32 v[48:49], 0
	v_mov_b64_e32 v[50:51], 0
	v_mov_b64_e32 v[52:53], 0
	v_mov_b64_e32 v[54:55], 0
	v_mov_b64_e32 v[56:57], 0
	v_mov_b64_e32 v[58:59], 0
	v_mov_b64_e32 v[60:61], 0
	v_mov_b64_e32 v[62:63], 0
	v_mov_b64_e32 v[64:65], 0
	v_mov_b64_e32 v[66:67], 0
	v_mov_b64_e32 v[68:69], 0
	v_mov_b64_e32 v[70:71], 0
	v_mov_b64_e32 v[72:73], 0
	v_mov_b64_e32 v[74:75], 0
	v_mov_b64_e32 v[76:77], 0
	v_mov_b64_e32 v[78:79], 0
	v_mov_b64_e32 v[80:81], 0
	v_mov_b64_e32 v[82:83], 0
	v_mov_b64_e32 v[84:85], 0
	v_mov_b64_e32 v[86:87], 0
	v_mov_b64_e32 v[88:89], 0
	v_mov_b64_e32 v[90:91], 0
	v_mov_b64_e32 v[92:93], 0
	v_mov_b64_e32 v[94:95], 0
	v_mov_b64_e32 v[96:97], 0
	v_mov_b64_e32 v[98:99], 0
	v_mov_b64_e32 v[100:101], 0
	v_mov_b64_e32 v[102:103], 0
	v_mov_b64_e32 v[104:105], 0
	v_mov_b64_e32 v[106:107], 0
	v_mov_b64_e32 v[108:109], 0
	v_mov_b64_e32 v[110:111], 0
	v_mov_b64_e32 v[112:113], 0
	v_mov_b64_e32 v[114:115], 0
	v_mov_b64_e32 v[116:117], 0
	v_mov_b64_e32 v[118:119], 0
	v_mov_b64_e32 v[120:121], 0
	v_mov_b64_e32 v[122:123], 0
	v_mov_b64_e32 v[124:125], 0
	v_mov_b64_e32 v[126:127], 0
